# background conversion task mapping generalized to the launch grid size (S = (bx-4) + (G-4) j); otherwise as the previous version
# baseline (speedup 1.0000x reference)
.Lm_bf3:
	s_cmp_lt_i32 s37, 0
	s_cbranch_scc1 .Lm_bs2
	s_sub_i32 s5, s82, 4
	s_mul_i32 s4, s83, s5
	s_add_i32 s4, s4, s37
	s_cmp_ge_u32 s4, 0xc000
	s_cbranch_scc1 .Lm_bs2
	s_cmp_ge_u32 s4, 0x8000
	s_cbranch_scc1 .Lm_dn4
	s_lshr_b32 s5, s4, 10
	s_bfe_u32 s6, s4, 0x40006
	s_and_b32 s7, s4, 63
	s_lshl_b32 s8, s6, 7
	s_lshl_b32 s9, s36, 4
	s_add_i32 s8, s8, s9
	s_lshl_b32 s10, s5, 25
	s_lshl_b32 s11, s8, 14
	s_add_i32 s10, s10, s11
	s_lshl_b32 s11, s7, 8
	s_add_i32 s10, s10, s11
	v_readlane_b32 s14, v237, 29
	v_readlane_b32 s15, v237, 30
	s_add_u32 s14, s14, s10
	s_addc_u32 s15, s15, 0
	s_mov_b32 s46, 0x4000
	s_bfe_u32 s10, s7, 0x40001
	s_lshl_b32 s10, s10, 8
	s_and_b32 s11, s7, 1
	s_lshl_b32 s11, s11, 6
	s_add_i32 s10, s10, s11
	s_lshr_b32 s11, s7, 5
	s_lshl_b32 s11, s11, 7
	s_add_i32 s10, s10, s11
	s_lshl_b32 s10, s10, 11
	s_add_i32 s10, s10, s8
	s_lshl_b32 s11, s5, 23
	s_add_i32 s10, s10, s11
	v_readlane_b32 s44, v237, 51
	v_readlane_b32 s45, v237, 52
	s_add_u32 s44, s44, s10
	s_addc_u32 s45, s45, 0
	s_branch .Lm_dd4
